# MLA steady loops: QK MFMAs reordered (chain A three deep first) so 8 of the 32 exps of a tile are deferred into the next tile's first QK gaps; PV gaps carry 3 exps each
# baseline (speedup 1.0000x reference)
; #define ISSUE_K(t, sl) do { glds16(Kg + (long)(t) * (KSLOT / 2), (unsigned)__builtin_amdgcn_readfirstlane(kdst + (sl) * KSLOT)); \
;         if (k2) glds16(Kg + (long)(t) * (KSLOT / 2) + 4096, (unsigned)__builtin_amdgcn_readfirstlane(kdst + (sl) * KSLOT + 8192)); } while (0)
; #define ISSUE_V(t, sl) glds16(Vg + (long)(t) * 4096, (unsigned)__builtin_amdgcn_readfirstlane(vdst + (sl) * VSLOT))
; #define SFENCE() __builtin_amdgcn_sched_barrier(0)
; template <bool FOX>
; __device__ __forceinline__ void attn_unit(const Args& A, int b, int h, int qb, LAS char* shm, LAS float* dg) {
;     ...
;     for (int t = 1; t < t_end; ++t) {
;         if (t == 1 && 4 < nti) ISSUE_K(t0 + 4, 0);
;         if (t + 4 < nti) ISSUE_K(t0 + t + 4, t % NS);
;         if (t + 2 < nti) ISSUE_V(t0 + t + 2, (t + 2) % NS);
;         SFENCE();
.LBB0_825:
	s_add_i32 s27, s26, 3
	s_cmp_lt_u32 s27, s94
	s_cbranch_scc0 .LBB0_828
	s_cmp_lg_u32 s98, 0
	s_cbranch_scc0 .Lmla_ss_no
	s_cmp_lg_u32 s26, s59
	s_cbranch_scc0 .Lmla_ss_no
	s_cmp_lg_u32 s26, 1
	s_cbranch_scc0 .Lmla_ss_no
	s_and_b32 s52, s27, 3
	s_mulk_i32 s52, 0x3000
	s_add_i32 s52, s52, s91
	s_add_i32 s53, s42, 0x6000
	s_and_b32 s53, s53, 0x6000
	s_add_i32 s53, s53, s93
	v_lshl_add_u64 v[250:251], v[232:233], 0, s[42:43]
	v_lshl_add_u64 v[240:241], v[234:235], 0, s[56:57]
	s_cmp_lt_i32 s89, 4
	s_cbranch_scc1 .Lmla_ss1_in
	s_branch .Lmla_ss2_top

; #define SFENCE() __builtin_amdgcn_sched_barrier(0)
; template <bool FOX>
; __device__ __forceinline__ void attn_unit(const Args& A, int b, int h, int qb, LAS char* shm, LAS float* dg) {
;     ...
;           const lds_cptr vp = vp0 + ((t - 1) % NS) * VSLOT; float sa = 0.f, sb = 0.f;
; #pragma unroll
;           for (int g = 0; g < 2 * NQ; ++g) {
;               if (!FOX && g == 0) c0 = __builtin_amdgcn_mfma_f32_32x32x16_bf16(kf[0], qr[0], negm, 0, 0, 0);
;               else if (!FOX && g == 1) c1 = __builtin_amdgcn_mfma_f32_32x32x16_bf16(kf[1], qr[0], negm, 0, 0, 0);
;               else if (g & 1) c1 = __builtin_amdgcn_mfma_f32_32x32x16_bf16(kf[g], qr[g >> 1], c1, 0, 0, 0); else c0 = __builtin_amdgcn_mfma_f32_32x32x16_bf16(kf[g], qr[g >> 1], c0, 0, 0, 0);
;               if (g < 8) { const int i = (g >> 1) + 4 * (g & 1); vlo[i] = vtr(vp + (i >> 2) * 4096 + (i & 3) * 1024); vhi[i] = vtr(vp + (i >> 2) * 4096 + (i & 3) * 1024 + 512);
;                   if (g < 4) { sa += pp0[4 * g]; sb += pp0[4 * g + 1]; sa += pp0[4 * g + 2]; sb += pp0[4 * g + 3]; } else { sa += pp1[4 * g - 16]; sb += pp1[4 * g - 15]; sa += pp1[4 * g - 14]; sb += pp1[4 * g - 13]; }
;                   asm volatile("" : "+v"(sa), "+v"(sb)); }
;               { constexpr int G0 = FOX ? 0 : 4; if (g >= G0) { const int q = 2 * (g - G0);
; #pragma unroll
;                   for (int k = 0; k < 2; ++k) { const int w = q + k; const unsigned pkd = w < 8 ? cvt_pk_bf16(pp0[2 * w], pp0[2 * w + 1]) : cvt_pk_bf16(pp1[2 * w - 16], pp1[2 * w - 15]); pw[w >> 2][w & 3] = pkd; } } }
;               SFENCE();
;           }
;           lrun += sa + sb; }
;         MASKONLY(t);
;         float rm; ROWMAX(rm);
;         bool resc = false;
;         if (__any(rm > THR)) { const float dl = fmaxf(rm, 0.f); mhat += dl;
; #pragma unroll
;             for (int r = 0; r < 16; ++r) { c0[r] -= dl; c1[r] -= dl; }
;             if constexpr (!FOX) {
; #pragma unroll
;                 for (int r = 0; r < 16; ++r) negm[r] = -mhat;
;                 asm volatile("" : "+v"(negm)); }
;             const float f = __builtin_amdgcn_exp2f(-dl); lrun *= f; if (hi == 0) wsf[r32] = f; resc = true; }
;         SFENCE();
;         { const lds_cptr kp = kp0 + ((t + 1) % NS) * KSLOT;
; #pragma unroll
;           for (int g = 0; g < 8; ++g) { const int i = (g >> 1) + 4 * (g & 1);
.Lmla_ss1_in:
	s_mov_b32 m0, s52
	s_nop 0
	global_load_lds_dwordx4 v[234:235], off
	s_add_i32 m0, s52, 0x2000
	s_nop 0
	global_load_lds_dwordx4 v[240:241], off
	s_mov_b32 m0, s53
	s_nop 0
	global_load_lds_dwordx4 v[250:251], off
	s_waitcnt lgkmcnt(0)
	s_add_i32 s27, s42, 0x8000
	v_mfma_f32_32x32x16_bf16 v[114:129], v[206:209], v[138:141], v[82:97]
	s_and_b32 s27, s27, 0x6000
	v_add_u32_e32 v3, s27, v247
	s_add_u32 s42, s42, 0x2000
	s_addc_u32 s43, s43, 0
	ds_read_b64_tr_b16 v[206:207], v3 offset:49152
	ds_read_b64_tr_b16 v[208:209], v3 offset:49664
	v_exp_f32_e32 v58, v106
	v_exp_f32_e32 v59, v107
	v_exp_f32_e32 v60, v108
	v_mfma_f32_32x32x16_bf16 v[114:129], v[202:205], v[142:145], v[114:129]
	ds_read_b64_tr_b16 v[202:203], v3 offset:50176
	ds_read_b64_tr_b16 v[204:205], v3 offset:50688
	v_exp_f32_e32 v61, v109
	v_exp_f32_e32 v62, v110
	v_exp_f32_e32 v63, v111
	v_mfma_f32_32x32x16_bf16 v[114:129], v[198:201], v[146:149], v[114:129]
	ds_read_b64_tr_b16 v[214:215], v3 offset:54272
	ds_read_b64_tr_b16 v[216:217], v3 offset:54784
	v_exp_f32_e32 v64, v112
	v_exp_f32_e32 v65, v113
	v_add_f32_e32 v4, 0, v67
	v_add_f32_e32 v5, 0, v66
	v_mfma_f32_32x32x16_bf16 v[98:113], v[194:197], v[138:141], v[82:97]
	ds_read_b64_tr_b16 v[194:195], v3 offset:53248
	ds_read_b64_tr_b16 v[196:197], v3 offset:53760
	v_add_f32_e32 v4, v69, v4
	v_add_f32_e32 v5, v68, v5
	v_add_f32_e32 v4, v71, v4
	v_add_f32_e32 v5, v70, v5
	v_add_f32_e32 v4, v73, v4
	v_add_f32_e32 v5, v72, v5
	v_mfma_f32_32x32x16_bf16 v[114:129], v[190:193], v[150:153], v[114:129]
	ds_read_b64_tr_b16 v[210:211], v3 offset:51200
	ds_read_b64_tr_b16 v[212:213], v3 offset:51712
	v_add_f32_e32 v4, v75, v4
	v_add_f32_e32 v5, v74, v5
	v_add_f32_e32 v4, v77, v4
	v_add_f32_e32 v5, v76, v5
	v_add_f32_e32 v4, v79, v4
	v_add_f32_e32 v5, v78, v5
	v_mfma_f32_32x32x16_bf16 v[98:113], v[186:189], v[142:145], v[98:113]
	ds_read_b64_tr_b16 v[12:13], v3 offset:55296
	ds_read_b64_tr_b16 v[14:15], v3 offset:55808
	v_add_f32_e32 v4, v81, v4
	v_add_f32_e32 v5, v80, v5
	v_add_f32_e32 v4, v51, v4
	v_add_f32_e32 v5, v50, v5
	v_add_f32_e32 v4, v53, v4
	v_add_f32_e32 v5, v52, v5
	v_mfma_f32_32x32x16_bf16 v[114:129], v[178:181], v[154:157], v[114:129]
	ds_read_b64_tr_b16 v[8:9], v3 offset:52224
	ds_read_b64_tr_b16 v[10:11], v3 offset:52736
	v_add_f32_e32 v4, v55, v4
	v_add_f32_e32 v5, v54, v5
	v_add_f32_e32 v4, v57, v4
	v_add_f32_e32 v5, v56, v5
	v_add_f32_e32 v4, v59, v4
	v_add_f32_e32 v16, v61, v4
	v_mfma_f32_32x32x16_bf16 v[98:113], v[182:185], v[146:149], v[98:113]
	v_add_f32_e32 v4, v58, v5
	v_add_f32_e32 v17, v60, v4
	ds_read_b64_tr_b16 v[4:5], v3 offset:56320
	ds_read_b64_tr_b16 v[6:7], v3 offset:56832
	v_add_f32_e32 v3, v63, v16
	v_add_f32_e32 v16, v62, v17
	v_add_f32_e32 v3, v65, v3
	v_add_f32_e32 v16, v64, v16
	v_mfma_f32_32x32x16_bf16 v[114:129], v[174:177], v[158:161], v[114:129]
	v_cvt_pk_bf16_f32 v178, v50, v51
	v_cvt_pk_bf16_f32 v179, v52, v53
	v_cvt_pk_bf16_f32 v186, v66, v67
	v_cvt_pk_bf16_f32 v187, v68, v69
	v_lshl_add_u64 v[234:235], v[234:235], 0, s[62:63]
	s_and_b32 s64, s26, 3
	s_mulk_i32 s64, 0x3000
	v_mfma_f32_32x32x16_bf16 v[98:113], v[170:173], v[150:153], v[98:113]
	v_cvt_pk_bf16_f32 v180, v54, v55
	v_cvt_pk_bf16_f32 v181, v56, v57
	v_cvt_pk_bf16_f32 v188, v70, v71
	v_cvt_pk_bf16_f32 v189, v72, v73
	v_lshl_add_u64 v[250:251], v[232:233], 0, s[42:43]
	s_add_i32 s52, s64, s91
	s_add_i32 s64, s42, 0x6000
	v_mfma_f32_32x32x16_bf16 v[98:113], v[166:169], v[154:157], v[98:113]
	v_cvt_pk_bf16_f32 v218, v58, v59
	v_cvt_pk_bf16_f32 v219, v60, v61
	v_cvt_pk_bf16_f32 v182, v74, v75
	v_cvt_pk_bf16_f32 v183, v76, v77
	v_lshl_add_u64 v[240:241], v[234:235], 0, s[56:57]
	s_and_b32 s64, s64, 0x6000
	s_add_i32 s53, s64, s93
	v_mfma_f32_32x32x16_bf16 v[98:113], v[162:165], v[158:161], v[98:113]
	v_cvt_pk_bf16_f32 v220, v62, v63
	v_cvt_pk_bf16_f32 v221, v64, v65
	v_cvt_pk_bf16_f32 v184, v78, v79
	v_cvt_pk_bf16_f32 v185, v80, v81
	v_add_f32_e32 v3, v3, v16
	v_add_f32_e32 v246, v246, v3
	s_nop 3
	s_waitcnt lgkmcnt(0)
	v_mfma_f32_32x32x16_bf16 v[18:33], v[186:189], v[206:209], v[18:33]
	s_add_i32 s27, s26, 1
	s_and_b32 s64, s27, 3
	s_mulk_i32 s64, 0x3000
	v_exp_f32_e32 v66, v114
	v_exp_f32_e32 v67, v115
	v_exp_f32_e32 v68, v116
	v_add_u32_e32 v3, s64, v248
	v_mfma_f32_32x32x16_bf16 v[34:49], v[186:189], v[194:197], v[34:49]
	v_exp_f32_e32 v69, v117
	v_exp_f32_e32 v70, v118
	v_exp_f32_e32 v71, v119
	ds_read_b128 v[206:209], v3
	ds_read_b128 v[194:197], v3 offset:512
	v_mfma_f32_32x32x16_bf16 v[18:33], v[182:185], v[202:205], v[18:33]
	v_exp_f32_e32 v72, v120
	v_exp_f32_e32 v73, v121
	v_exp_f32_e32 v74, v122
	ds_read_b128 v[202:205], v3 offset:2048
	ds_read_b128 v[186:189], v3 offset:2560
	v_mfma_f32_32x32x16_bf16 v[34:49], v[182:185], v[214:217], v[34:49]
	v_exp_f32_e32 v75, v123
	v_exp_f32_e32 v76, v124
	v_exp_f32_e32 v77, v125
	ds_read_b128 v[198:201], v3 offset:4096
	ds_read_b128 v[182:185], v3 offset:4608
	v_mfma_f32_32x32x16_bf16 v[18:33], v[178:181], v[210:213], v[18:33]
	v_exp_f32_e32 v78, v126
	v_exp_f32_e32 v79, v127
	v_exp_f32_e32 v80, v128
	ds_read_b128 v[190:193], v3 offset:6144
	ds_read_b128 v[170:173], v3 offset:6656
	v_mfma_f32_32x32x16_bf16 v[34:49], v[178:181], v[12:15], v[34:49]
	v_exp_f32_e32 v81, v129
	v_exp_f32_e32 v50, v98
	v_exp_f32_e32 v51, v99
	ds_read_b128 v[178:181], v3 offset:8192
	ds_read_b128 v[166:169], v3 offset:8704
	v_mfma_f32_32x32x16_bf16 v[18:33], v[218:221], v[8:11], v[18:33]
	v_exp_f32_e32 v52, v100
	v_exp_f32_e32 v53, v101
	v_exp_f32_e32 v54, v102
	ds_read_b128 v[174:177], v3 offset:10240
	ds_read_b128 v[162:165], v3 offset:10752
	v_mfma_f32_32x32x16_bf16 v[34:49], v[218:221], v[4:7], v[34:49]
	v_exp_f32_e32 v55, v103
	v_exp_f32_e32 v56, v104
	v_exp_f32_e32 v57, v105
	s_mov_b32 s26, s27
	s_cmp_eq_u32 s27, s96
	s_cbranch_scc1 .Lmla_ss1_xdone
	s_add_i32 s64, s27, 3
	s_cmp_lt_u32 s64, s94
	s_cbranch_scc1 .Lmla_ss1_top
	s_waitcnt vmcnt(4)
	s_barrier
	s_branch .Lmla_ss_back

; #define SFENCE() __builtin_amdgcn_sched_barrier(0)
; template <bool FOX>
; __device__ __forceinline__ void attn_unit(const Args& A, int b, int h, int qb, LAS char* shm, LAS float* dg) {
;     ...
;           const lds_cptr vp = vp0 + ((t - 1) % NS) * VSLOT; float sa = 0.f, sb = 0.f;
; #pragma unroll
;           for (int g = 0; g < 2 * NQ; ++g) {
;               if (!FOX && g == 0) c0 = __builtin_amdgcn_mfma_f32_32x32x16_bf16(kf[0], qr[0], negm, 0, 0, 0);
;               else if (!FOX && g == 1) c1 = __builtin_amdgcn_mfma_f32_32x32x16_bf16(kf[1], qr[0], negm, 0, 0, 0);
;               else if (g & 1) c1 = __builtin_amdgcn_mfma_f32_32x32x16_bf16(kf[g], qr[g >> 1], c1, 0, 0, 0); else c0 = __builtin_amdgcn_mfma_f32_32x32x16_bf16(kf[g], qr[g >> 1], c0, 0, 0, 0);
;               if (g < 8) { const int i = (g >> 1) + 4 * (g & 1); vlo[i] = vtr(vp + (i >> 2) * 4096 + (i & 3) * 1024); vhi[i] = vtr(vp + (i >> 2) * 4096 + (i & 3) * 1024 + 512);
;                   if (g < 4) { sa += pp0[4 * g]; sb += pp0[4 * g + 1]; sa += pp0[4 * g + 2]; sb += pp0[4 * g + 3]; } else { sa += pp1[4 * g - 16]; sb += pp1[4 * g - 15]; sa += pp1[4 * g - 14]; sb += pp1[4 * g - 13]; }
;                   asm volatile("" : "+v"(sa), "+v"(sb)); }
;               { constexpr int G0 = FOX ? 0 : 4; if (g >= G0) { const int q = 2 * (g - G0);
; #pragma unroll
;                   for (int k = 0; k < 2; ++k) { const int w = q + k; const unsigned pkd = w < 8 ? cvt_pk_bf16(pp0[2 * w], pp0[2 * w + 1]) : cvt_pk_bf16(pp1[2 * w - 16], pp1[2 * w - 15]); pw[w >> 2][w & 3] = pkd; } } }
;               SFENCE();
;           }
;           lrun += sa + sb; }
;         MASKONLY(t);
;         float rm; ROWMAX(rm);
;         bool resc = false;
;         if (__any(rm > THR)) { const float dl = fmaxf(rm, 0.f); mhat += dl;
; #pragma unroll
;             for (int r = 0; r < 16; ++r) { c0[r] -= dl; c1[r] -= dl; }
;             if constexpr (!FOX) {
; #pragma unroll
;                 for (int r = 0; r < 16; ++r) negm[r] = -mhat;
;                 asm volatile("" : "+v"(negm)); }
;             const float f = __builtin_amdgcn_exp2f(-dl); lrun *= f; if (hi == 0) wsf[r32] = f; resc = true; }
;         SFENCE();
;         { const lds_cptr kp = kp0 + ((t + 1) % NS) * KSLOT;
; #pragma unroll
;           for (int g = 0; g < 8; ++g) { const int i = (g >> 1) + 4 * (g & 1);
.Lmla_ss2_top:
	s_mov_b32 m0, s52
	s_nop 0
	global_load_lds_dwordx4 v[234:235], off
	s_mov_b32 m0, s53
	s_nop 0
	global_load_lds_dwordx4 v[250:251], off
	s_waitcnt lgkmcnt(0)
	s_add_i32 s27, s42, 0x8000
	v_mfma_f32_32x32x16_bf16 v[114:129], v[206:209], v[138:141], v[82:97]
	s_and_b32 s27, s27, 0x6000
	v_add_u32_e32 v3, s27, v247
	s_add_u32 s42, s42, 0x2000
	s_addc_u32 s43, s43, 0
	ds_read_b64_tr_b16 v[206:207], v3 offset:49152
	ds_read_b64_tr_b16 v[208:209], v3 offset:49664
	v_exp_f32_e32 v58, v106
	v_exp_f32_e32 v59, v107
	v_exp_f32_e32 v60, v108
	v_mfma_f32_32x32x16_bf16 v[114:129], v[202:205], v[142:145], v[114:129]
	ds_read_b64_tr_b16 v[202:203], v3 offset:50176
	ds_read_b64_tr_b16 v[204:205], v3 offset:50688
	v_exp_f32_e32 v61, v109
	v_exp_f32_e32 v62, v110
	v_exp_f32_e32 v63, v111
	v_mfma_f32_32x32x16_bf16 v[114:129], v[198:201], v[146:149], v[114:129]
	ds_read_b64_tr_b16 v[214:215], v3 offset:54272
	ds_read_b64_tr_b16 v[216:217], v3 offset:54784
	v_exp_f32_e32 v64, v112
	v_exp_f32_e32 v65, v113
	v_add_f32_e32 v4, 0, v67
	v_add_f32_e32 v5, 0, v66
	v_mfma_f32_32x32x16_bf16 v[98:113], v[194:197], v[138:141], v[82:97]
	ds_read_b64_tr_b16 v[194:195], v3 offset:53248
	ds_read_b64_tr_b16 v[196:197], v3 offset:53760
	v_add_f32_e32 v4, v69, v4
	v_add_f32_e32 v5, v68, v5
	v_add_f32_e32 v4, v71, v4
	v_add_f32_e32 v5, v70, v5
	v_add_f32_e32 v4, v73, v4
	v_add_f32_e32 v5, v72, v5
	v_mfma_f32_32x32x16_bf16 v[114:129], v[190:193], v[150:153], v[114:129]
	ds_read_b64_tr_b16 v[210:211], v3 offset:51200
	ds_read_b64_tr_b16 v[212:213], v3 offset:51712
	v_add_f32_e32 v4, v75, v4
	v_add_f32_e32 v5, v74, v5
	v_add_f32_e32 v4, v77, v4
	v_add_f32_e32 v5, v76, v5
	v_add_f32_e32 v4, v79, v4
	v_add_f32_e32 v5, v78, v5
	v_mfma_f32_32x32x16_bf16 v[98:113], v[186:189], v[142:145], v[98:113]
	ds_read_b64_tr_b16 v[12:13], v3 offset:55296
	ds_read_b64_tr_b16 v[14:15], v3 offset:55808
	v_add_f32_e32 v4, v81, v4
	v_add_f32_e32 v5, v80, v5
	v_add_f32_e32 v4, v51, v4
	v_add_f32_e32 v5, v50, v5
	v_add_f32_e32 v4, v53, v4
	v_add_f32_e32 v5, v52, v5
	v_mfma_f32_32x32x16_bf16 v[114:129], v[178:181], v[154:157], v[114:129]
	ds_read_b64_tr_b16 v[8:9], v3 offset:52224
	ds_read_b64_tr_b16 v[10:11], v3 offset:52736
	v_add_f32_e32 v4, v55, v4
	v_add_f32_e32 v5, v54, v5
	v_add_f32_e32 v4, v57, v4
	v_add_f32_e32 v5, v56, v5
	v_add_f32_e32 v4, v59, v4
	v_add_f32_e32 v16, v61, v4
	v_mfma_f32_32x32x16_bf16 v[98:113], v[182:185], v[146:149], v[98:113]
	v_add_f32_e32 v4, v58, v5
	v_add_f32_e32 v17, v60, v4
	ds_read_b64_tr_b16 v[4:5], v3 offset:56320
	ds_read_b64_tr_b16 v[6:7], v3 offset:56832
	v_add_f32_e32 v3, v63, v16
	v_add_f32_e32 v16, v62, v17
	v_add_f32_e32 v3, v65, v3
	v_add_f32_e32 v16, v64, v16
	v_mfma_f32_32x32x16_bf16 v[114:129], v[174:177], v[158:161], v[114:129]
	v_cvt_pk_bf16_f32 v178, v50, v51
	v_cvt_pk_bf16_f32 v179, v52, v53
	v_cvt_pk_bf16_f32 v186, v66, v67
	v_cvt_pk_bf16_f32 v187, v68, v69
	v_lshl_add_u64 v[234:235], v[234:235], 0, s[62:63]
	s_and_b32 s64, s26, 3
	s_mulk_i32 s64, 0x3000
	v_mfma_f32_32x32x16_bf16 v[98:113], v[170:173], v[150:153], v[98:113]
	v_cvt_pk_bf16_f32 v180, v54, v55
	v_cvt_pk_bf16_f32 v181, v56, v57
	v_cvt_pk_bf16_f32 v188, v70, v71
	v_cvt_pk_bf16_f32 v189, v72, v73
	v_lshl_add_u64 v[250:251], v[232:233], 0, s[42:43]
	s_add_i32 s52, s64, s91
	s_add_i32 s64, s42, 0x6000
	v_mfma_f32_32x32x16_bf16 v[98:113], v[166:169], v[154:157], v[98:113]
	v_cvt_pk_bf16_f32 v218, v58, v59
	v_cvt_pk_bf16_f32 v219, v60, v61
	v_cvt_pk_bf16_f32 v182, v74, v75
	v_cvt_pk_bf16_f32 v183, v76, v77
	s_and_b32 s64, s64, 0x6000
	s_add_i32 s53, s64, s93
	v_mfma_f32_32x32x16_bf16 v[98:113], v[162:165], v[158:161], v[98:113]
	v_cvt_pk_bf16_f32 v220, v62, v63
	v_cvt_pk_bf16_f32 v221, v64, v65
	v_cvt_pk_bf16_f32 v184, v78, v79
	v_cvt_pk_bf16_f32 v185, v80, v81
	v_add_f32_e32 v3, v3, v16
	v_add_f32_e32 v246, v246, v3
	s_waitcnt vmcnt(3)
	s_waitcnt lgkmcnt(0)
	s_barrier
	v_mfma_f32_32x32x16_bf16 v[18:33], v[186:189], v[206:209], v[18:33]
	s_add_i32 s27, s26, 1
	s_and_b32 s64, s27, 3
	s_mulk_i32 s64, 0x3000
	v_exp_f32_e32 v66, v114
	v_exp_f32_e32 v67, v115
	v_exp_f32_e32 v68, v116
	v_add_u32_e32 v3, s64, v248
	v_mfma_f32_32x32x16_bf16 v[34:49], v[186:189], v[194:197], v[34:49]
	v_exp_f32_e32 v69, v117
	v_exp_f32_e32 v70, v118
	v_exp_f32_e32 v71, v119
	ds_read_b128 v[206:209], v3
	ds_read_b128 v[194:197], v3 offset:512
	v_mfma_f32_32x32x16_bf16 v[18:33], v[182:185], v[202:205], v[18:33]
	v_exp_f32_e32 v72, v120
	v_exp_f32_e32 v73, v121
	v_exp_f32_e32 v74, v122
	ds_read_b128 v[202:205], v3 offset:2048
	ds_read_b128 v[186:189], v3 offset:2560
	v_mfma_f32_32x32x16_bf16 v[34:49], v[182:185], v[214:217], v[34:49]
	v_exp_f32_e32 v75, v123
	v_exp_f32_e32 v76, v124
	v_exp_f32_e32 v77, v125
	ds_read_b128 v[198:201], v3 offset:4096
	ds_read_b128 v[182:185], v3 offset:4608
	v_mfma_f32_32x32x16_bf16 v[18:33], v[178:181], v[210:213], v[18:33]
	v_exp_f32_e32 v78, v126
	v_exp_f32_e32 v79, v127
	v_exp_f32_e32 v80, v128
	ds_read_b128 v[190:193], v3 offset:6144
	ds_read_b128 v[170:173], v3 offset:6656
	v_mfma_f32_32x32x16_bf16 v[34:49], v[178:181], v[12:15], v[34:49]
	v_exp_f32_e32 v81, v129
	v_exp_f32_e32 v50, v98
	v_exp_f32_e32 v51, v99
	ds_read_b128 v[178:181], v3 offset:8192
	ds_read_b128 v[166:169], v3 offset:8704
	v_mfma_f32_32x32x16_bf16 v[18:33], v[218:221], v[8:11], v[18:33]
	v_exp_f32_e32 v52, v100
	v_exp_f32_e32 v53, v101
	v_exp_f32_e32 v54, v102
	ds_read_b128 v[174:177], v3 offset:10240
	ds_read_b128 v[162:165], v3 offset:10752
	v_mfma_f32_32x32x16_bf16 v[34:49], v[218:221], v[4:7], v[34:49]
	v_exp_f32_e32 v55, v103
	v_exp_f32_e32 v56, v104
	v_exp_f32_e32 v57, v105
	s_mov_b32 s26, s27
	s_cmp_eq_u32 s27, s96
	s_cbranch_scc1 .Lmla_ss2_xdone
	s_add_i32 s64, s27, 3
	s_cmp_lt_u32 s64, s94
	s_cbranch_scc1 .Lmla_ss2_top
	s_branch .Lmla_ss_back

; template <bool FOX>
; __device__ __forceinline__ void attn_unit(const Args& A, int b, int h, int qb, LAS char* shm, LAS float* dg) {
;     ...
;         { const lds_cptr kp = kp0 + ((t + 1) % NS) * KSLOT;
; #pragma unroll
;           for (int g = 0; g < 8; ++g) { const int i = (g >> 1) + 4 * (g & 1);
;               const bf16x8 vf = (bf16x8){vlo[i][0], vlo[i][1], vlo[i][2], vlo[i][3], vhi[i][0], vhi[i][1], vhi[i][2], vhi[i][3]};
;               o[g & 1] = __builtin_amdgcn_mfma_f32_32x32x16_bf16(__builtin_bit_cast(bf16x8, pw[g >> 1]), vf, o[g & 1], 0, 0, 0);
;               if (g < 4) {
; #pragma unroll
;                   for (int k = 0; k < 4; ++k) pp0[4 * g + k] = __builtin_amdgcn_exp2f(c0[4 * g + k]);
;                   asm volatile("" : "+v"(pp0)); }
;               else {
; #pragma unroll
;                   for (int k = 0; k < 4; ++k) pp1[4 * g - 16 + k] = __builtin_amdgcn_exp2f(c1[4 * g - 16 + k]);
;                   asm volatile("" : "+v"(pp1)); }
.Lmla_ss_back:
	v_exp_f32_e32 v58, v106
	v_exp_f32_e32 v59, v107
	v_exp_f32_e32 v60, v108
	v_exp_f32_e32 v61, v109
	v_exp_f32_e32 v62, v110
	v_exp_f32_e32 v63, v111
	v_exp_f32_e32 v64, v112
	v_exp_f32_e32 v65, v113
	s_waitcnt lgkmcnt(0)
	s_mov_b64 s[60:61], 0
	s_branch .LBB0_825
.Lmla_ss_done:
	v_exp_f32_e32 v58, v106
	v_exp_f32_e32 v59, v107
	v_exp_f32_e32 v60, v108
	v_exp_f32_e32 v61, v109
	v_exp_f32_e32 v62, v110
	v_exp_f32_e32 v63, v111
	v_exp_f32_e32 v64, v112
	v_exp_f32_e32 v65, v113
	s_waitcnt lgkmcnt(0)
	s_mov_b64 s[46:47], -1
	s_mov_b64 s[52:53], -1
	s_mov_b64 s[60:61], 0
	s_branch .LBB0_867
